# k_sort: all kernarg loads issued up front (late scalar loads were stalling its write-out)
# speedup vs baseline: 1.0500x; 1.0023x over previous
_Z6k_sortPKfS0_PKiS2_PiP15HIP_vector_typeIfLj4EEPfS7_S3_S7_S7_S3_S3_S6_S6_:
	s_load_dwordx2 s[4:5], s[0:1], 0x70
	s_load_dwordx8 s[8:15], s[0:1], 0x0
	s_load_dwordx8 s[36:43], s[0:1], 0x40
	s_load_dwordx2 s[44:45], s[0:1], 0x60
	s_load_dwordx2 s[46:47], s[0:1], 0x20
	s_load_dwordx4 s[48:51], s[0:1], 0x30
	s_mov_b32 s17, 0
	s_mov_b32 s16, s17
	v_lshl_or_b32 v2, s2, 12, v0
	v_mov_b32_e32 v3, 0
	s_mov_b32 s18, s17
	s_mov_b32 s19, s17
	v_mov_b64_e32 v[6:7], s[16:17]
	s_waitcnt lgkmcnt(0)
	v_lshl_add_u64 v[4:5], v[2:3], 4, s[4:5]
	v_mov_b64_e32 v[8:9], s[18:19]
	global_store_dwordx4 v[4:5], v[6:9], off
	v_or_b32_e32 v4, 0x400, v2
	v_mov_b32_e32 v5, v3
	v_lshl_add_u64 v[4:5], v[4:5], 4, s[4:5]
	global_store_dwordx4 v[4:5], v[6:9], off
	v_or_b32_e32 v4, 0x800, v2
	v_mov_b32_e32 v5, v3
	v_lshl_add_u64 v[4:5], v[4:5], 4, s[4:5]
	v_or_b32_e32 v2, 0xc00, v2
	s_movk_i32 s3, 0x100
	global_store_dwordx4 v[4:5], v[6:9], off
	v_lshl_add_u64 v[4:5], v[2:3], 4, s[4:5]
	v_cmp_gt_u32_e64 s[6:7], s3, v0
	global_store_dwordx4 v[4:5], v[6:9], off
	s_and_saveexec_b64 s[4:5], s[6:7]
	v_mov_b32_e32 v1, 0x10400
	v_lshl_add_u32 v1, v0, 2, v1
	ds_write_b32 v1, v3
	s_or_b64 exec, exec, s[4:5]
	s_lshr_b32 s28, s2, 1
	s_and_b32 s18, s2, 1
	s_bitcmp1_b32 s2, 0
	s_cselect_b64 s[2:3], -1, 0
	s_lshl_b32 s16, s28, 12
	s_lshl_b64 s[4:5], s[16:17], 3
	s_cmp_eq_u32 s18, 0
	s_cselect_b32 s8, s8, s10
	s_cselect_b32 s9, s9, s11
	s_cselect_b32 s10, s12, s14
	s_cselect_b32 s11, s13, s15
	s_add_u32 s4, s8, s4
	v_or_b32_e32 v13, 0x400, v0
	s_addc_u32 s5, s9, s5
	v_lshlrev_b32_e32 v1, 3, v0
	v_lshlrev_b32_e32 v2, 3, v13
	v_or_b32_e32 v12, 0x800, v0
	global_load_dwordx2 v[8:9], v1, s[4:5]
	global_load_dwordx2 v[4:5], v2, s[4:5]
	v_lshlrev_b32_e32 v2, 3, v12
	v_or_b32_e32 v10, 0xc00, v0
	global_load_dwordx2 v[6:7], v2, s[4:5]
	v_lshlrev_b32_e32 v2, 3, v10
	global_load_dwordx2 v[2:3], v2, s[4:5]
	s_lshl_b64 s[4:5], s[16:17], 2
	s_add_u32 s4, s10, s4
	s_addc_u32 s5, s11, s5
	v_lshlrev_b32_e32 v11, 2, v0
	v_lshlrev_b32_e32 v14, 2, v13
	global_load_dword v17, v11, s[4:5]
	global_load_dword v16, v14, s[4:5]
	v_lshlrev_b32_e32 v14, 2, v12
	global_load_dword v15, v14, s[4:5]
	v_lshlrev_b32_e32 v14, 2, v10
	global_load_dword v14, v14, s[4:5]
	v_mov_b32_e32 v20, 0
	ds_write2st64_b32 v11, v20, v20 offset0:192 offset1:208
	ds_write2st64_b32 v11, v20, v20 offset0:224 offset1:240
	v_mov_b32_e32 v18, 0xff
	v_mov_b32_e32 v25, 0x10400
	v_mov_b32_e32 v19, 1
	s_waitcnt lgkmcnt(0)
	s_barrier
	v_cmp_gt_u32_e32 vcc, 64, v0
	s_waitcnt vmcnt(7)
	v_mul_f32_e32 v20, 0x43800000, v8
	s_waitcnt vmcnt(6)
	v_mul_f32_e32 v21, 0x43800000, v4
	v_cvt_i32_f32_e32 v20, v20
	v_cvt_i32_f32_e32 v21, v21
	s_waitcnt vmcnt(5)
	v_mul_f32_e32 v22, 0x43800000, v6
	v_cvt_i32_f32_e32 v22, v22
	s_waitcnt vmcnt(4)
	v_mul_f32_e32 v23, 0x43800000, v2
	v_cvt_i32_f32_e32 v23, v23
	v_med3_i32 v26, v20, 0, v18
	v_med3_i32 v20, v21, 0, v18
	v_med3_i32 v22, v22, 0, v18
	v_med3_i32 v24, v23, 0, v18
	v_lshl_add_u32 v21, v26, 2, v25
	v_lshl_add_u32 v23, v20, 2, v25
	v_lshl_add_u32 v28, v22, 2, v25
	ds_add_rtn_u32 v27, v21, v19
	ds_add_rtn_u32 v21, v23, v19
	ds_add_rtn_u32 v23, v28, v19
	v_lshl_add_u32 v25, v24, 2, v25
	ds_add_rtn_u32 v25, v25, v19
	s_waitcnt lgkmcnt(0)
	s_barrier
	s_and_saveexec_b64 s[4:5], vcc
	s_cbranch_execz .LBB0_4
	v_lshlrev_b32_e32 v33, 4, v0
	v_add_u32_e32 v28, 0x10400, v33
	ds_read_b128 v[28:31], v28
	v_mov_b32_e32 v32, 0
	s_waitcnt lgkmcnt(0)
	v_add_u32_e32 v34, v29, v28
	v_add3_u32 v31, v34, v30, v31
	s_nop 1
	v_add_u32_dpp v34, v31, v31 row_shr:1 row_mask:0xf bank_mask:0xf bound_ctrl:1
	s_nop 1
	v_add_u32_dpp v34, v34, v34 row_shr:2 row_mask:0xf bank_mask:0xf bound_ctrl:1
	s_nop 1
	v_add_u32_dpp v34, v34, v34 row_shr:4 row_mask:0xf bank_mask:0xf bound_ctrl:1
	s_nop 1
	v_add_u32_dpp v34, v34, v34 row_shr:8 row_mask:0xf bank_mask:0xf bound_ctrl:1
	s_nop 1
	v_add_u32_dpp v34, v34, v34 row_bcast:15 row_mask:0xa bank_mask:0xf
	s_nop 1
	v_mov_b32_dpp v32, v34 row_bcast:31 row_mask:0xc bank_mask:0xf
	v_sub_u32_e32 v31, v32, v31
	v_add_u32_e32 v32, v31, v34
	v_or_b32_e32 v31, 0x10000, v33
	v_add_u32_e32 v33, v32, v28
	v_add_u32_e32 v34, v33, v29
	v_add_u32_e32 v35, v34, v30
	ds_write_b128 v31, v[32:35]

.LBB0_6:
	s_or_b64 exec, exec, s[4:5]
	s_waitcnt lgkmcnt(0)
	s_barrier
	ds_read_b32 v19, v29
	v_lshl_add_u32 v26, v26, s8, v27
	ds_read_b32 v27, v30
	ds_read_b32 v28, v28
	ds_read_b32 v25, v25
	s_waitcnt vmcnt(3)
	v_cmp_eq_u32_e32 vcc, 0, v17
	s_mov_b64 s[4:5], -1
	s_waitcnt lgkmcnt(3)
	v_add_lshl_u32 v19, v26, v19, 2
	ds_write2st64_b32 v19, v8, v9 offset1:64
	v_bfrev_b32_e32 v8, 1
	v_cndmask_b32_e32 v8, 0, v8, vcc
	v_or_b32_e32 v8, v8, v0
	ds_write_b32 v19, v8 offset:32768
	v_lshl_add_u32 v8, v20, s8, v21
	s_waitcnt lgkmcnt(4)
	v_add_lshl_u32 v8, v8, v27, 2
	ds_write2st64_b32 v8, v4, v5 offset1:64
	v_mov_b32_e32 v4, 0x400
	v_mov_b32_e32 v5, 0x80000400
	s_waitcnt vmcnt(2)
	v_cmp_eq_u32_e32 vcc, 0, v16
	s_nop 1
	v_cndmask_b32_e32 v4, v4, v5, vcc
	v_or_b32_e32 v4, v4, v0
	ds_write_b32 v8, v4 offset:32768
	v_lshl_add_u32 v4, v22, s8, v23
	s_waitcnt lgkmcnt(5)
	v_add_lshl_u32 v4, v4, v28, 2
	ds_write2st64_b32 v4, v6, v7 offset1:64
	v_mov_b32_e32 v5, 0x800
	v_mov_b32_e32 v6, 0x80000800
	s_waitcnt vmcnt(1)
	v_cmp_eq_u32_e32 vcc, 0, v15
	s_nop 1
	v_cndmask_b32_e32 v5, v5, v6, vcc
	v_or_b32_e32 v5, v5, v0
	ds_write_b32 v4, v5 offset:32768
	v_lshl_add_u32 v4, v24, s8, v18
	s_waitcnt lgkmcnt(6)
	v_add_lshl_u32 v4, v4, v25, 2
	ds_write2st64_b32 v4, v2, v3 offset1:64
	v_mov_b32_e32 v2, 0xc00
	v_mov_b32_e32 v3, 0x80000c00
	s_waitcnt vmcnt(0)
	v_cmp_eq_u32_e32 vcc, 0, v14
	s_nop 1
	v_cndmask_b32_e32 v2, v2, v3, vcc
	v_or_b32_e32 v2, v2, v0
	ds_write_b32 v4, v2 offset:32768
	s_waitcnt lgkmcnt(0)
	s_barrier
	s_getpc_b64 s[30:31]
	s_add_u32 s30, s30, 0x24b8
	s_addc_u32 s31, s31, 0
	v_lshlrev_b32_e32 v40, 6, v0
	v_min_u32_e32 v40, 0x2d00, v40
	global_load_dword v40, v40, s[30:31]
	ds_read_b32 v14, v11 offset:32768
	s_mov_b64 s[18:19], s[44:45]
	s_mov_b64 s[8:9], s[36:37]
	s_mov_b64 s[10:11], s[38:39]
	s_mov_b64 s[12:13], s[40:41]
	s_mov_b64 s[14:15], s[42:43]
	ds_read2st64_b32 v[4:5], v11 offset1:64
	v_or_b32_e32 v2, s16, v0
	v_mov_b32_e32 v3, 0
	s_waitcnt lgkmcnt(0)
	v_and_b32_e32 v15, 0x7fffffff, v14
	s_and_b64 vcc, exec, s[2:3]
	v_lshlrev_b64 v[6:7], 2, v[2:3]
	s_cbranch_vccz .LBB0_8
	v_lshl_add_u64 v[8:9], s[10:11], 0, v[6:7]
	global_store_dword v[8:9], v4, off
	v_lshl_add_u64 v[8:9], s[12:13], 0, v[6:7]
	global_store_dword v[8:9], v5, off
	v_lshl_add_u64 v[8:9], s[14:15], 0, v[6:7]
	global_store_dword v[8:9], v15, off
	s_mov_b64 s[4:5], 0
.LBB0_8:
	s_mov_b64 s[24:25], s[46:47]
	s_mov_b64 s[20:21], s[48:49]
	s_mov_b64 s[22:23], s[50:51]
	v_or_b32_e32 v8, 0x4000, v11
	v_or_b32_e32 v9, 0x8000, v11
	s_andn2_b64 vcc, exec, s[4:5]
	s_mov_b64 s[4:5], s[18:19]
	s_cbranch_vccnz .LBB0_10
	s_waitcnt lgkmcnt(0)
	v_lshl_add_u64 v[16:17], s[24:25], 0, v[6:7]
	global_store_dword v[16:17], v15, off
	v_lshl_add_u64 v[16:17], s[20:21], 0, v[6:7]
	v_lshl_add_u64 v[6:7], s[22:23], 0, v[6:7]
	s_mov_b64 s[4:5], s[8:9]
	global_store_dword v[16:17], v4, off
	global_store_dword v[6:7], v5, off

	.amdhsa_kernel _Z6k_sortPKfS0_PKiS2_PiP15HIP_vector_typeIfLj4EEPfS7_S3_S7_S7_S3_S3_S6_S6_
		.amdhsa_group_segment_fixed_size 67584
		.amdhsa_private_segment_fixed_size 0
		.amdhsa_kernarg_size 120
		.amdhsa_user_sgpr_count 2
		.amdhsa_user_sgpr_dispatch_ptr 0
		.amdhsa_user_sgpr_queue_ptr 0
		.amdhsa_user_sgpr_kernarg_segment_ptr 1
		.amdhsa_user_sgpr_dispatch_id 0
		.amdhsa_user_sgpr_kernarg_preload_length 0
		.amdhsa_user_sgpr_kernarg_preload_offset 0
		.amdhsa_user_sgpr_private_segment_size 0
		.amdhsa_uses_dynamic_stack 0
		.amdhsa_enable_private_segment 0
		.amdhsa_system_sgpr_workgroup_id_x 1
		.amdhsa_system_sgpr_workgroup_id_y 0
		.amdhsa_system_sgpr_workgroup_id_z 0
		.amdhsa_system_sgpr_workgroup_info 0
		.amdhsa_system_vgpr_workitem_id 0
		.amdhsa_next_free_vgpr 48
		.amdhsa_next_free_sgpr 52
		.amdhsa_accum_offset 48
		.amdhsa_reserve_vcc 1
		.amdhsa_float_round_mode_32 0
		.amdhsa_float_round_mode_16_64 0
		.amdhsa_float_denorm_mode_32 3
		.amdhsa_float_denorm_mode_16_64 3
		.amdhsa_dx10_clamp 1
		.amdhsa_ieee_mode 1
		.amdhsa_fp16_overflow 0
		.amdhsa_tg_split 0
		.amdhsa_exception_fp_ieee_invalid_op 0
		.amdhsa_exception_fp_denorm_src 0
		.amdhsa_exception_fp_ieee_div_zero 0
		.amdhsa_exception_fp_ieee_overflow 0
		.amdhsa_exception_fp_ieee_underflow 0
		.amdhsa_exception_fp_ieee_inexact 0
		.amdhsa_exception_int_div_zero 0
	.end_amdhsa_kernel

amdhsa.kernels:
  - .agpr_count:     0
    .args:
      - .actual_access:  read_only
        .address_space:  global
        .offset:         0
        .size:           8
        .value_kind:     global_buffer
      - .actual_access:  read_only
        .address_space:  global
        .offset:         8
        .size:           8
        .value_kind:     global_buffer
      - .actual_access:  read_only
        .address_space:  global
        .offset:         16
        .size:           8
        .value_kind:     global_buffer
      - .actual_access:  read_only
        .address_space:  global
        .offset:         24
        .size:           8
        .value_kind:     global_buffer
      - .actual_access:  write_only
        .address_space:  global
        .offset:         32
        .size:           8
        .value_kind:     global_buffer
      - .actual_access:  write_only
        .address_space:  global
        .offset:         40
        .size:           8
        .value_kind:     global_buffer
      - .actual_access:  write_only
        .address_space:  global
        .offset:         48
        .size:           8
        .value_kind:     global_buffer
      - .actual_access:  write_only
        .address_space:  global
        .offset:         56
        .size:           8
        .value_kind:     global_buffer
      - .actual_access:  write_only
        .address_space:  global
        .offset:         64
        .size:           8
        .value_kind:     global_buffer
      - .actual_access:  write_only
        .address_space:  global
        .offset:         72
        .size:           8
        .value_kind:     global_buffer
      - .actual_access:  write_only
        .address_space:  global
        .offset:         80
        .size:           8
        .value_kind:     global_buffer
      - .actual_access:  write_only
        .address_space:  global
        .offset:         88
        .size:           8
        .value_kind:     global_buffer
      - .actual_access:  write_only
        .address_space:  global
        .offset:         96
        .size:           8
        .value_kind:     global_buffer
      - .actual_access:  write_only
        .address_space:  global
        .offset:         104
        .size:           8
        .value_kind:     global_buffer
      - .actual_access:  write_only
        .address_space:  global
        .offset:         112
        .size:           8
        .value_kind:     global_buffer
    .group_segment_fixed_size: 67584
    .kernarg_segment_align: 8
    .kernarg_segment_size: 120
    .language:       OpenCL C
    .language_version:
      - 2
      - 0
    .max_flat_workgroup_size: 1024
    .name:           _Z6k_sortPKfS0_PKiS2_PiP15HIP_vector_typeIfLj4EEPfS7_S3_S7_S7_S3_S3_S6_S6_
    .private_segment_fixed_size: 0
    .sgpr_count:     58
    .sgpr_spill_count: 0
    .symbol:         _Z6k_sortPKfS0_PKiS2_PiP15HIP_vector_typeIfLj4EEPfS7_S3_S7_S7_S3_S3_S6_S6_.kd
    .uniform_work_group_size: 1
    .uses_dynamic_stack: false
    .vgpr_count:     48
    .vgpr_spill_count: 0
    .wavefront_size: 64
  - .agpr_count:     0
    .args:
      - .actual_access:  read_only
        .address_space:  global
        .offset:         0
        .size:           8
        .value_kind:     global_buffer
      - .actual_access:  read_only
        .address_space:  global
        .offset:         8
        .size:           8
        .value_kind:     global_buffer
      - .actual_access:  read_only
        .address_space:  global
        .offset:         16
        .size:           8
        .value_kind:     global_buffer
      - .actual_access:  read_only
        .address_space:  global
        .offset:         24
        .size:           8
        .value_kind:     global_buffer
      - .actual_access:  read_only
        .address_space:  global
        .offset:         32
        .size:           8
        .value_kind:     global_buffer
      - .actual_access:  read_only
        .address_space:  global
        .offset:         40
        .size:           8
        .value_kind:     global_buffer
      - .actual_access:  read_only
        .address_space:  global
        .offset:         48
        .size:           8
        .value_kind:     global_buffer
      - .actual_access:  write_only
        .address_space:  global
        .offset:         56
        .size:           8
        .value_kind:     global_buffer
    .group_segment_fixed_size: 145952
    .kernarg_segment_align: 8
    .kernarg_segment_size: 64
    .language:       OpenCL C
    .language_version:
      - 2
      - 0
    .max_flat_workgroup_size: 512
    .name:           _Z7k_finalPK15HIP_vector_typeIfLj4EES2_PKiS4_PKfS6_PKDF16_Pf
    .private_segment_fixed_size: 0
    .sgpr_count:     34
    .sgpr_spill_count: 0
    .symbol:         _Z7k_finalPK15HIP_vector_typeIfLj4EES2_PKiS4_PKfS6_PKDF16_Pf.kd
    .uniform_work_group_size: 1
    .uses_dynamic_stack: false
    .vgpr_count:     177
    .vgpr_spill_count: 0
    .wavefront_size: 64
  - .agpr_count:     0
    .args:
      - .actual_access:  read_only
        .address_space:  global
        .offset:         0
        .size:           8
        .value_kind:     global_buffer
      - .actual_access:  read_only
        .address_space:  global
        .offset:         8
        .size:           8
        .value_kind:     global_buffer
      - .actual_access:  read_only
        .address_space:  global
        .offset:         16
        .size:           8
        .value_kind:     global_buffer
      - .actual_access:  read_only
        .address_space:  global
        .offset:         24
        .size:           8
        .value_kind:     global_buffer
      - .actual_access:  read_only
        .address_space:  global
        .offset:         32
        .size:           8
        .value_kind:     global_buffer
      - .actual_access:  read_only
        .address_space:  global
        .offset:         40
        .size:           8
        .value_kind:     global_buffer
      - .actual_access:  read_only
        .address_space:  global
        .offset:         48
        .size:           8
        .value_kind:     global_buffer
      - .actual_access:  read_only
        .address_space:  global
        .offset:         56
        .size:           8
        .value_kind:     global_buffer
      - .actual_access:  read_only
        .address_space:  global
        .offset:         64
        .size:           8
        .value_kind:     global_buffer
      - .address_space:  global
        .offset:         72
        .size:           8
        .value_kind:     global_buffer
      - .actual_access:  read_only
        .address_space:  global
        .offset:         80
        .size:           8
        .value_kind:     global_buffer
      - .actual_access:  read_only
        .address_space:  global
        .offset:         88
        .size:           8
        .value_kind:     global_buffer
      - .actual_access:  read_only
        .address_space:  global
        .offset:         96
        .size:           8
        .value_kind:     global_buffer
      - .actual_access:  write_only
        .address_space:  global
        .offset:         104
        .size:           8
        .value_kind:     global_buffer
      - .address_space:  global
        .offset:         112
        .size:           8
        .value_kind:     global_buffer
      - .actual_access:  write_only
        .address_space:  global
        .offset:         120
        .size:           8
        .value_kind:     global_buffer
      - .actual_access:  write_only
        .address_space:  global
        .offset:         128
        .size:           8
        .value_kind:     global_buffer
      - .actual_access:  write_only
        .address_space:  global
        .offset:         136
        .size:           8
        .value_kind:     global_buffer
      - .actual_access:  write_only
        .address_space:  global
        .offset:         144
        .size:           8
        .value_kind:     global_buffer
    .group_segment_fixed_size: 30384
    .kernarg_segment_align: 8
    .kernarg_segment_size: 152
    .language:       OpenCL C
    .language_version:
      - 2
      - 0
    .max_flat_workgroup_size: 512
    .name:           _Z6k_iterILb1ELb0EEvPKfS1_PKiPK15HIP_vector_typeIfLj4EES7_S1_S1_S3_S1_PfS8_S1_S3_PDF16_PS5_SA_PiSA_SB_
    .private_segment_fixed_size: 0
    .sgpr_count:     102
    .sgpr_spill_count: 0
    .symbol:         _Z6k_iterILb1ELb0EEvPKfS1_PKiPK15HIP_vector_typeIfLj4EES7_S1_S1_S3_S1_PfS8_S1_S3_PDF16_PS5_SA_PiSA_SB_.kd
    .uniform_work_group_size: 1
    .uses_dynamic_stack: false
    .vgpr_count:     216
    .vgpr_spill_count: 0
    .wavefront_size: 64
  - .agpr_count:     0
    .args:
      - .actual_access:  read_only
        .address_space:  global
        .offset:         0
        .size:           8
        .value_kind:     global_buffer
      - .actual_access:  read_only
        .address_space:  global
        .offset:         8
        .size:           8
        .value_kind:     global_buffer
      - .actual_access:  read_only
        .address_space:  global
        .offset:         16
        .size:           8
        .value_kind:     global_buffer
      - .actual_access:  read_only
        .address_space:  global
        .offset:         24
        .size:           8
        .value_kind:     global_buffer
      - .actual_access:  read_only
        .address_space:  global
        .offset:         32
        .size:           8
        .value_kind:     global_buffer
      - .actual_access:  read_only
        .address_space:  global
        .offset:         40
        .size:           8
        .value_kind:     global_buffer
      - .actual_access:  read_only
        .address_space:  global
        .offset:         48
        .size:           8
        .value_kind:     global_buffer
      - .actual_access:  read_only
        .address_space:  global
        .offset:         56
        .size:           8
        .value_kind:     global_buffer
      - .actual_access:  read_only
        .address_space:  global
        .offset:         64
        .size:           8
        .value_kind:     global_buffer
      - .address_space:  global
        .offset:         72
        .size:           8
        .value_kind:     global_buffer
      - .actual_access:  read_only
        .address_space:  global
        .offset:         80
        .size:           8
        .value_kind:     global_buffer
      - .actual_access:  read_only
        .address_space:  global
        .offset:         88
        .size:           8
        .value_kind:     global_buffer
      - .actual_access:  read_only
        .address_space:  global
        .offset:         96
        .size:           8
        .value_kind:     global_buffer
      - .actual_access:  read_only
        .address_space:  global
        .offset:         104
        .size:           8
        .value_kind:     global_buffer
      - .actual_access:  read_only
        .address_space:  global
        .offset:         112
        .size:           8
        .value_kind:     global_buffer
      - .actual_access:  read_only
        .address_space:  global
        .offset:         120
        .size:           8
        .value_kind:     global_buffer
      - .actual_access:  read_only
        .address_space:  global
        .offset:         128
        .size:           8
        .value_kind:     global_buffer
      - .actual_access:  read_only
        .address_space:  global
        .offset:         136
        .size:           8
        .value_kind:     global_buffer
      - .actual_access:  read_only
        .address_space:  global
        .offset:         144
        .size:           8
        .value_kind:     global_buffer
    .group_segment_fixed_size: 5808
    .kernarg_segment_align: 8
    .kernarg_segment_size: 152
    .language:       OpenCL C
    .language_version:
      - 2
      - 0
    .max_flat_workgroup_size: 512
    .name:           _Z6k_iterILb0ELb0EEvPKfS1_PKiPK15HIP_vector_typeIfLj4EES7_S1_S1_S3_S1_PfS8_S1_S3_PDF16_PS5_SA_PiSA_SB_
    .private_segment_fixed_size: 0
    .sgpr_count:     46
    .sgpr_spill_count: 0
    .symbol:         _Z6k_iterILb0ELb0EEvPKfS1_PKiPK15HIP_vector_typeIfLj4EES7_S1_S1_S3_S1_PfS8_S1_S3_PDF16_PS5_SA_PiSA_SB_.kd
    .uniform_work_group_size: 1
    .uses_dynamic_stack: false
    .vgpr_count:     184
    .vgpr_spill_count: 0
    .wavefront_size: 64
  - .agpr_count:     0
    .args:
      - .actual_access:  read_only
        .address_space:  global
        .offset:         0
        .size:           8
        .value_kind:     global_buffer
      - .actual_access:  read_only
        .address_space:  global
        .offset:         8
        .size:           8
        .value_kind:     global_buffer
      - .actual_access:  read_only
        .address_space:  global
        .offset:         16
        .size:           8
        .value_kind:     global_buffer
      - .actual_access:  read_only
        .address_space:  global
        .offset:         24
        .size:           8
        .value_kind:     global_buffer
      - .actual_access:  read_only
        .address_space:  global
        .offset:         32
        .size:           8
        .value_kind:     global_buffer
      - .actual_access:  read_only
        .address_space:  global
        .offset:         40
        .size:           8
        .value_kind:     global_buffer
      - .actual_access:  read_only
        .address_space:  global
        .offset:         48
        .size:           8
        .value_kind:     global_buffer
      - .actual_access:  read_only
        .address_space:  global
        .offset:         56
        .size:           8
        .value_kind:     global_buffer
      - .actual_access:  read_only
        .address_space:  global
        .offset:         64
        .size:           8
        .value_kind:     global_buffer
      - .address_space:  global
        .offset:         72
        .size:           8
        .value_kind:     global_buffer
      - .actual_access:  write_only
        .address_space:  global
        .offset:         80
        .size:           8
        .value_kind:     global_buffer
      - .actual_access:  read_only
        .address_space:  global
        .offset:         88
        .size:           8
        .value_kind:     global_buffer
      - .actual_access:  read_only
        .address_space:  global
        .offset:         96
        .size:           8
        .value_kind:     global_buffer
      - .actual_access:  read_only
        .address_space:  global
        .offset:         104
        .size:           8
        .value_kind:     global_buffer
      - .actual_access:  read_only
        .address_space:  global
        .offset:         112
        .size:           8
        .value_kind:     global_buffer
      - .actual_access:  read_only
        .address_space:  global
        .offset:         120
        .size:           8
        .value_kind:     global_buffer
      - .actual_access:  read_only
        .address_space:  global
        .offset:         128
        .size:           8
        .value_kind:     global_buffer
      - .actual_access:  read_only
        .address_space:  global
        .offset:         136
        .size:           8
        .value_kind:     global_buffer
      - .actual_access:  read_only
        .address_space:  global
        .offset:         144
        .size:           8
        .value_kind:     global_buffer
    .group_segment_fixed_size: 5808
    .kernarg_segment_align: 8
    .kernarg_segment_size: 152
    .language:       OpenCL C
    .language_version:
      - 2
      - 0
    .max_flat_workgroup_size: 512
    .name:           _Z6k_iterILb0ELb1EEvPKfS1_PKiPK15HIP_vector_typeIfLj4EES7_S1_S1_S3_S1_PfS8_S1_S3_PDF16_PS5_SA_PiSA_SB_
    .private_segment_fixed_size: 0
    .sgpr_count:     46
    .sgpr_spill_count: 0
    .symbol:         _Z6k_iterILb0ELb1EEvPKfS1_PKiPK15HIP_vector_typeIfLj4EES7_S1_S1_S3_S1_PfS8_S1_S3_PDF16_PS5_SA_PiSA_SB_.kd
    .uniform_work_group_size: 1
    .uses_dynamic_stack: false
    .vgpr_count:     184
    .vgpr_spill_count: 0
    .wavefront_size: 64
